# expert-up: tile->expert map and tile count kept in SGPRs (no per-unit loads/drains) + epilogue load hoists
# speedup vs baseline: 1.0034x; 1.0034x over previous
; #define PG8_STAGE(bufoff, gbase, voff) do { _Pragma("unroll") for (int _i = 0; _i < 2; ++_i) \
;         __builtin_amdgcn_global_load_lds((const unsigned*)((const char*)(gbase) + (voff)[_i]), (LAS unsigned*)(lds + (bufoff) + ldsw + _i * 8192), 16, 0, 0); } while (0)
; #define PG8_WAIT_V(n) asm volatile("s_waitcnt vmcnt(" #n ")" ::: "memory")
; #define PG8_BAR __builtin_amdgcn_s_barrier()
;     ...
;     const char* cA = cur.A; const char* cB = cur.B;
;     if constexpr (SP2) {
;         PG8_STAGE(PG8_SB(0, 0), cB, voffB); PG8_STAGE(PG8_SB(0, 1), cB + hstep, voffB); PG8_STAGE(PG8_SA(0, 0), cA, voffA); PG8_STAGE(PG8_SA(0, 1), cA + hstep, voffA);
;         if (wr == 1) PG8_BAR;
;         PG8_WAIT_V(2); PG8_BAR;
;         PG8_STAGE(PG8_SB(1, 0), cB + kstep, voffB); PG8_STAGE(PG8_SA(1, 0), cA + kstep, voffA); PG8_STAGE(PG8_SB(1, 1), cB + hstep + kstep, voffB);
;         PG8_WAIT_V(6); PG8_BAR;
;     __device__ __forceinline__ bool next(int i, pg8::Unit& u) const {
;         const int T = tiles[0]; const long Lx = (long)i * G + c; if (Lx >= (long)T * nN) return false;
;         pg8::tile_of((int)Lx, T, nN, u.pm, u.pn); const int e = tiles[1 + u.pm]; u.z = e;
;         u.A = A0 + (size_t)u.pm * tsA; u.B = B0 + (size_t)e * estride + (size_t)u.pn * tsB; return true;
;     }
.LBB0_2249:
	s_movk_i32 s0, 0x800
	v_mov_b32_e32 v163, 0
	global_load_dword v1, v163, s[10:11]
	s_ashr_i32 s3, s2, 31
	v_readfirstlane_b32 s4, v0
	s_waitcnt vmcnt(0) lgkmcnt(0)
	v_mul_hi_i32 v3, v1, 56
	v_mul_lo_u32 v2, v1, 56
	v_cmp_ge_i64_e32 vcc, s[2:3], v[2:3]
	v_readfirstlane_b32 s1, v1
	s_cbranch_vccnz .LBB0_2266
	v_and_b32_e32 v248, 63, v0
	v_lshlrev_b32_e32 v249, 2, v248
	global_load_dword v250, v249, s[10:11] offset:4
	global_load_dword v251, v249, s[10:11] offset:260
	v_add_u32_e32 v252, 64, v248
	s_mov_b32 s100, 0
	s_mov_b32 s101, 0
	s_waitcnt vmcnt(0)
	v_cmp_gt_u32_e32 vcc, s1, v248
	s_nop 1
	v_cndmask_b32_e32 v250, 8, v250, vcc
	v_cmp_gt_u32_e32 vcc, s1, v252
	s_nop 1
	v_cndmask_b32_e32 v251, 8, v251, vcc
	v_cmp_gt_u32_e32 vcc, 1, v250
	s_bcnt1_i32_b64 s20, vcc
	v_cmp_gt_u32_e32 vcc, 1, v251
	s_bcnt1_i32_b64 s21, vcc
	s_add_u32 s20, s20, s21
	s_mov_b32 s21, 0
	s_or_b64 s[100:101], s[100:101], s[20:21]
	v_cmp_gt_u32_e32 vcc, 2, v250
	s_bcnt1_i32_b64 s20, vcc
	v_cmp_gt_u32_e32 vcc, 2, v251
	s_bcnt1_i32_b64 s21, vcc
	s_add_u32 s20, s20, s21
	s_mov_b32 s21, 0
	s_lshl_b64 s[20:21], s[20:21], 7
	s_or_b64 s[100:101], s[100:101], s[20:21]
	v_cmp_gt_u32_e32 vcc, 3, v250
	s_bcnt1_i32_b64 s20, vcc
	v_cmp_gt_u32_e32 vcc, 3, v251
	s_bcnt1_i32_b64 s21, vcc
	s_add_u32 s20, s20, s21
	s_mov_b32 s21, 0
	s_lshl_b64 s[20:21], s[20:21], 14
	s_or_b64 s[100:101], s[100:101], s[20:21]
	v_cmp_gt_u32_e32 vcc, 4, v250
	s_bcnt1_i32_b64 s20, vcc
	v_cmp_gt_u32_e32 vcc, 4, v251
	s_bcnt1_i32_b64 s21, vcc
	s_add_u32 s20, s20, s21
	s_mov_b32 s21, 0
	s_lshl_b64 s[20:21], s[20:21], 21
	s_or_b64 s[100:101], s[100:101], s[20:21]
	v_cmp_gt_u32_e32 vcc, 5, v250
	s_bcnt1_i32_b64 s20, vcc
	v_cmp_gt_u32_e32 vcc, 5, v251
	s_bcnt1_i32_b64 s21, vcc
	s_add_u32 s20, s20, s21
	s_mov_b32 s21, 0
	s_lshl_b64 s[20:21], s[20:21], 28
	s_or_b64 s[100:101], s[100:101], s[20:21]
	v_cmp_gt_u32_e32 vcc, 6, v250
	s_bcnt1_i32_b64 s20, vcc
	v_cmp_gt_u32_e32 vcc, 6, v251
	s_bcnt1_i32_b64 s21, vcc
	s_add_u32 s20, s20, s21
	s_mov_b32 s21, 0
	s_lshl_b64 s[20:21], s[20:21], 35
	s_or_b64 s[100:101], s[100:101], s[20:21]
	v_cmp_gt_u32_e32 vcc, 7, v250
	s_bcnt1_i32_b64 s20, vcc
	v_cmp_gt_u32_e32 vcc, 7, v251
	s_bcnt1_i32_b64 s21, vcc
	s_add_u32 s20, s20, s21
	s_mov_b32 s21, 0
	s_lshl_b64 s[20:21], s[20:21], 42
	s_or_b64 s[100:101], s[100:101], s[20:21]
	s_mov_b32 s20, s1
	s_mov_b32 s21, 0
	s_lshl_b64 s[20:21], s[20:21], 49
	s_or_b64 s[100:101], s[100:101], s[20:21]
	s_add_u32 s16, s52, 0xde00000
	s_addc_u32 s17, s53, 0
	s_lshr_b32 s21, s3, 29
	s_add_i32 s21, s2, s21
	s_and_b32 s22, s21, -8
	s_sub_i32 s22, s2, s22
	s_mul_i32 s20, s1, 7
	s_lshr_b32 s23, s22, 31
	s_add_i32 s20, s20, s23
	s_mul_i32 s20, s20, s22
	s_ashr_i32 s21, s21, 3
	s_add_i32 s22, s20, s21
	s_mul_hi_i32 s20, s22, 0x92492493
	s_add_i32 s20, s20, s22
	s_lshr_b32 s21, s20, 31
	s_ashr_i32 s20, s20, 8
	s_add_i32 s23, s20, s21
	s_lshl_b32 s24, s23, 3
	s_sub_i32 s1, s1, s24
	s_min_i32 s25, s1, 8
	s_abs_i32 s29, s25
	v_cvt_f32_u32_e32 v1, s29
	s_sub_i32 s36, 0, s29
	s_mulk_i32 s23, 0x1c0
	s_sub_i32 s22, s22, s23
	v_rcp_iflag_f32_e32 v1, v1
	s_abs_i32 s35, s22
	s_lshr_b32 s5, s4, 6
	s_ashr_i32 s1, s0, 31
	v_mul_f32_e32 v1, 0x4f7ffffe, v1
	v_cvt_u32_f32_e32 v1, v1
	s_xor_b32 s23, s22, s25
	s_lshr_b32 s28, s4, 8
	s_lshl_b64 s[20:21], s[0:1], 7
	v_readfirstlane_b32 s37, v1
	s_mul_i32 s36, s36, s37
	s_mul_hi_u32 s36, s37, s36
	s_add_i32 s37, s37, s36
	s_mul_hi_u32 s36, s35, s37
	s_mul_i32 s37, s36, s29
	s_sub_i32 s35, s35, s37
	s_lshl_b32 s34, s5, 10
	s_ashr_i32 s23, s23, 31
	s_add_i32 s37, s36, 1
	s_sub_i32 s38, s35, s29
	s_cmp_ge_u32 s35, s29
	s_cselect_b32 s36, s37, s36
	s_cselect_b32 s35, s38, s35
	s_add_i32 s37, s36, 1
	s_cmp_ge_u32 s35, s29
	s_cselect_b32 s29, s37, s36
	s_xor_b32 s29, s29, s23
	s_sub_i32 s48, s29, s23
	s_mul_i32 s23, s48, s25
	s_sub_i32 s22, s22, s23
	s_add_i32 s62, s24, s22
	s_ashr_i32 s63, s62, 31
	s_lshl_b64 s[22:23], s[62:63], 2
	s_add_u32 s22, s10, s22
	s_addc_u32 s23, s11, s23
	global_load_dword v1, v163, s[22:23] offset:4
	v_lshlrev_b32_e32 v2, 4, v0
	v_lshrrev_b32_e32 v3, 3, v0
	s_movk_i32 s22, 0x70
	v_and_b32_e32 v4, 32, v0
	v_bfe_u32 v16, v0, 2, 4
	v_and_b32_e32 v17, 64, v0
	v_bitop3_b32 v19, v3, s22, 64 bitop3:0xc8
	v_bitop3_b32 v18, v2, v4, 48 bitop3:0x6c
	v_and_b32_e32 v20, 48, v3
	v_or_b32_e32 v3, v19, v16
	v_or_b32_e32 v2, v18, v17
	v_or_b32_e32 v4, v20, v16
	v_mad_u64_u32 v[164:165], s[22:23], s0, v3, v[2:3]
	v_mad_u64_u32 v[4:5], s[22:23], s0, v4, v[2:3]
	s_lshl_b64 s[22:23], s[62:63], 19
	s_mov_b32 s35, 0x3800000
	s_add_u32 s64, s42, s22
	s_addc_u32 s65, s43, s23
	s_ashr_i32 s49, s48, 31
	s_lshl_b64 s[22:23], s[48:49], 19
	s_add_i32 s44, s34, 0
	s_add_i32 m0, s44, 0x10000
	s_add_i32 s45, s44, 0x2000
	v_mov_b32_e32 v162, v4
	v_mov_b32_e32 v165, v163
	s_mov_b32 s51, 0
	v_lshl_add_u64 v[10:11], s[64:65], 0, v[164:165]
	s_waitcnt vmcnt(0)
	v_mul_hi_i32 v3, v1, s35
	v_mul_lo_u32 v2, v1, s35
	v_lshl_add_u64 v[2:3], s[16:17], 0, v[2:3]
	v_lshl_add_u64 v[2:3], v[2:3], 0, s[22:23]
	v_lshl_add_u64 v[8:9], v[2:3], 0, s[20:21]
	v_readfirstlane_b32 s22, v2
	v_readfirstlane_b32 s23, v3
	v_readfirstlane_b32 s24, v8
	v_readfirstlane_b32 s25, v9
	v_lshl_add_u64 v[14:15], v[2:3], 0, v[162:163]
	v_lshl_add_u64 v[12:13], v[2:3], 0, v[164:165]
	v_lshl_add_u64 v[6:7], v[8:9], 0, v[162:163]
	global_load_lds_dwordx4 v4, s[22:23]
	s_add_i32 m0, s44, 0x12000
	s_nop 0
	global_load_lds_dwordx4 v164, s[22:23]
	s_add_i32 m0, s44, 0x14000
	s_nop 0
	global_load_lds_dwordx4 v4, s[24:25]
	s_add_i32 m0, s44, 0x16000
	s_add_u32 s22, s64, s20
	global_load_lds_dwordx4 v164, s[24:25]
	s_mov_b32 m0, s44
	s_addc_u32 s23, s65, s21
	global_load_lds_dwordx4 v4, s[64:65]
	s_add_i32 s49, s44, 0x4000
	s_mov_b32 m0, s45
	s_add_i32 s50, s44, 0x6000
	global_load_lds_dwordx4 v164, s[64:65]
	s_mov_b32 m0, s49
	s_cmp_eq_u32 s28, 1
	global_load_lds_dwordx4 v4, s[22:23]
	s_mov_b32 m0, s50
	v_lshl_add_u64 v[4:5], v[8:9], 0, v[164:165]
	global_load_lds_dwordx4 v164, s[22:23]
	v_lshl_add_u64 v[8:9], s[64:65], 0, v[162:163]
	s_cselect_b64 s[22:23], -1, 0
	s_cmp_lg_u32 s28, 1
	s_cbranch_scc1 .LBB0_2252
	s_barrier

;     ...
;         const bool has_next = S.next(ui + 1, nxt);
;         const char* nA = has_next ? nxt.A : cA; const char* nB = has_next ? nxt.B : cB;
;     __device__ __forceinline__ bool next(int i, pg8::Unit& u) const {
;         const int T = tiles[0]; const long Lx = (long)i * G + c; if (Lx >= (long)T * nN) return false;
;         pg8::tile_of((int)Lx, T, nN, u.pm, u.pn); const int e = tiles[1 + u.pm]; u.z = e;
;         u.A = A0 + (size_t)u.pm * tsA; u.B = B0 + (size_t)e * estride + (size_t)u.pn * tsB; return true;
;     }
.LBB0_2255:
	s_add_i32 s51, s51, 1
	s_mul_i32 s4, s51, s68
	s_mul_hi_u32 s5, s51, s33
	s_mul_i32 s39, s51, s33
	s_add_i32 s5, s5, s4
	s_add_u32 s66, s39, s2
	s_addc_u32 s67, s5, s3
	s_bfe_u64 s[38:39], s[100:101], 0x70031
	s_mov_b32 s39, s38
	v_mov_b32_e32 v4, s38
	v_mul_hi_i32 v5, v4, 56
	v_mul_lo_u32 v4, v4, 56
	v_cmp_ge_i64_e32 vcc, s[66:67], v[4:5]
	v_cmp_lt_i64_e64 s[4:5], s[66:67], v[4:5]
	s_cbranch_vccnz .LBB0_2257
	s_ashr_i32 s40, s66, 31
	s_lshr_b32 s40, s40, 29
	s_add_i32 s40, s66, s40
	s_ashr_i32 s41, s40, 3
	s_and_b32 s40, s40, -8
	s_sub_i32 s40, s66, s40
	s_mul_i32 s38, s39, 7
	s_lshr_b32 s46, s40, 31
	s_add_i32 s38, s38, s46
	s_mul_i32 s38, s40, s38
	s_add_i32 s38, s38, s41
	s_mul_hi_i32 s40, s38, 0x92492493
	s_add_i32 s40, s40, s38
	s_lshr_b32 s41, s40, 31
	s_ashr_i32 s40, s40, 8
	s_add_i32 s40, s40, s41
	s_lshl_b32 s41, s40, 3
	s_sub_i32 s39, s39, s41
	s_min_i32 s39, s39, 8
	s_abs_i32 s46, s39
	v_cvt_f32_u32_e32 v4, s46
	s_sub_i32 s66, 0, s46
	s_mulk_i32 s40, 0x1c0
	s_sub_i32 s40, s38, s40
	v_rcp_iflag_f32_e32 v4, v4
	s_abs_i32 s38, s40
	s_xor_b32 s47, s40, s39
	s_ashr_i32 s47, s47, 31
	v_mul_f32_e32 v4, 0x4f7ffffe, v4
	v_cvt_u32_f32_e32 v4, v4
	s_nop 0
	v_readfirstlane_b32 s67, v4
	s_mul_i32 s66, s66, s67
	s_mul_hi_u32 s66, s67, s66
	s_add_i32 s67, s67, s66
	s_mul_hi_u32 s66, s38, s67
	s_mul_i32 s67, s66, s46
	s_sub_i32 s38, s38, s67
	s_add_i32 s67, s66, 1
	s_sub_i32 s72, s38, s46
	s_cmp_ge_u32 s38, s46
	s_cselect_b32 s66, s67, s66
	s_cselect_b32 s38, s72, s38
	s_add_i32 s67, s66, 1
	s_cmp_ge_u32 s38, s46
	s_cselect_b32 s38, s67, s66
	s_xor_b32 s38, s38, s47
	s_sub_i32 s38, s38, s47
	s_mul_i32 s39, s38, s39
	s_sub_i32 s39, s40, s39
	s_add_i32 s40, s41, s39
	s_ashr_i32 s41, s40, 31
	s_lshl_b64 s[46:47], s[40:41], 2
	s_add_u32 s46, s10, s46
	s_addc_u32 s47, s11, s47
	s_mov_b32 s66, 0
	s_bfe_u64 s[46:47], s[100:101], 0x70000
	s_cmp_ge_u32 s40, s46
	s_addc_u32 s66, s66, 0
	s_bfe_u64 s[46:47], s[100:101], 0x70007
	s_cmp_ge_u32 s40, s46
	s_addc_u32 s66, s66, 0
	s_bfe_u64 s[46:47], s[100:101], 0x7000e
	s_cmp_ge_u32 s40, s46
	s_addc_u32 s66, s66, 0
	s_bfe_u64 s[46:47], s[100:101], 0x70015
	s_cmp_ge_u32 s40, s46
	s_addc_u32 s66, s66, 0
	s_bfe_u64 s[46:47], s[100:101], 0x7001c
	s_cmp_ge_u32 s40, s46
	s_addc_u32 s66, s66, 0
	s_bfe_u64 s[46:47], s[100:101], 0x70023
	s_cmp_ge_u32 s40, s46
	s_addc_u32 s66, s66, 0
	s_bfe_u64 s[46:47], s[100:101], 0x7002a
	s_cmp_ge_u32 s40, s46
	s_addc_u32 s66, s66, 0
	v_mov_b32_e32 v4, s66
	s_lshl_b64 s[46:47], s[40:41], 19
	s_add_u32 s46, s42, s46
	s_addc_u32 s47, s43, s47
	s_ashr_i32 s39, s38, 31
	s_lshl_b64 s[66:67], s[38:39], 19
	v_mul_hi_i32 v5, v4, s35
	v_mul_lo_u32 v4, v4, s35
	v_lshl_add_u64 v[4:5], s[16:17], 0, v[4:5]
	v_lshl_add_u64 v[172:173], v[4:5], 0, s[66:67]
